# grid barriers: L1 invalidate (buffer_inv sc1) issued while waiting for the release instead of after it (no loads in between on this CU)
# speedup vs baseline: 1.0285x; 1.0131x over previous
; __device__ __forceinline__ unsigned xb_ld(unsigned* p)              { return __hip_atomic_load(p, __ATOMIC_RELAXED, __HIP_MEMORY_SCOPE_AGENT); }
; __device__ __forceinline__ unsigned xb_add(unsigned* p, unsigned v) { return __hip_atomic_fetch_add(p, v, __ATOMIC_RELAXED, __HIP_MEMORY_SCOPE_AGENT); }
; #define XB_SPIN(cond, bar) do { unsigned _sp = 0; while (cond) { __builtin_amdgcn_s_sleep(1); \
;     if ((++_sp & 255u) == 0u) { if (xb_ld(&(bar)[XB_TMO])) break; if (_sp > XB_SPIN_CAP) { atomicAdd(&(bar)[XB_TMO], 1u); break; } } } } while (0)
; __device__ __forceinline__ void xcd_barrier(const XcdBarrier& b, int wave_id, int pair = -1) {
;     ...
;         const unsigned old = xb_add(&bar[XB_XSUB(b.x)], 1u);
;         const unsigned gen = old / nloc;
;         if (old + 1u == (gen + 1u) * nloc) {
;             __builtin_amdgcn_fence(__ATOMIC_RELEASE, "agent");
;             asm volatile("s_waitcnt vmcnt(0)" ::: "memory");
;             unsigned* topw = pair < 0 ? &bar[XB_TOP] : &bar[XB_PTOP(pair)]; unsigned* topg = pair < 0 ? &bar[XB_TOPGEN] : &bar[XB_PTOPGEN(pair)];
;             if (pair >= 0) nx = 2u;
;             const unsigned og = xb_add(topw, 1u);
;             const unsigned tg = og / nx;
;             if (og + 1u == (tg + 1u) * nx) xb_add(topg, 1u);
;             else XB_SPIN(xb_ld(topg) == tg, bar);
;             __builtin_amdgcn_fence(__ATOMIC_ACQUIRE, "agent");
;             xb_add(&bar[XB_XGEN(b.x)], 1u);
;             asm volatile("s_waitcnt vmcnt(0)" ::: "memory");
;         } else {
;             XB_SPIN(xb_ld(&bar[XB_XGEN(b.x)]) == gen, bar);
;             __builtin_amdgcn_fence(__ATOMIC_ACQUIRE, "agent");
;             asm volatile("s_waitcnt vmcnt(0)" ::: "memory");
.LBB0_74:
	s_or_b64 exec, exec, s[10:11]
	v_cvt_f32_u32_e32 v4, v2
	s_waitcnt vmcnt(0)
	v_readfirstlane_b32 s3, v3
	v_sub_u32_e32 v3, 0, v2
	v_rcp_iflag_f32_e32 v4, v4
	v_add_u32_e32 v5, s3, v1
	v_mul_f32_e32 v4, 0x4f7ffffe, v4
	v_cvt_u32_f32_e32 v4, v4
	v_mul_lo_u32 v1, v3, v4
	v_mul_hi_u32 v1, v4, v1
	v_add_u32_e32 v1, v4, v1
	v_mul_hi_u32 v1, v5, v1
	v_mul_lo_u32 v3, v1, v2
	v_sub_u32_e32 v3, v5, v3
	v_add_u32_e32 v4, 1, v1
	v_cmp_ge_u32_e32 vcc, v3, v2
	s_nop 1
	v_cndmask_b32_e32 v1, v1, v4, vcc
	v_sub_u32_e32 v4, v3, v2
	v_cndmask_b32_e32 v3, v3, v4, vcc
	v_add_u32_e32 v4, 1, v1
	v_cmp_ge_u32_e32 vcc, v3, v2
	v_add_u32_e32 v3, 1, v5
	s_nop 0
	v_cndmask_b32_e32 v1, v1, v4, vcc
	v_mul_lo_u32 v4, v2, v1
	v_add_u32_e32 v2, v4, v2
	v_cmp_ne_u32_e32 vcc, v3, v2
	s_and_saveexec_b64 s[8:9], vcc
	s_xor_b64 s[8:9], exec, s[8:9]
	s_cbranch_execz .LBB0_88
	s_waitcnt lgkmcnt(0)
	buffer_inv sc1
	v_mov_b32_e32 v0, 0x2000
	global_load_dword v0, v0, s[6:7] offset:1024 sc1
	s_add_u32 s14, s6, 0x2400
	s_addc_u32 s15, s7, 0
	s_waitcnt vmcnt(0)
	v_cmp_eq_u32_e32 vcc, v0, v1
	s_and_saveexec_b64 s[10:11], vcc
	s_cbranch_execz .LBB0_87
	s_add_u32 s12, s30, 0x4200
	s_addc_u32 s13, s31, 0
	s_mov_b32 s3, 1
	s_mov_b64 s[16:17], 0
	v_mov_b32_e32 v0, 0
	s_branch .LBB0_78

; __device__ __forceinline__ unsigned xb_ld(unsigned* p)              { return __hip_atomic_load(p, __ATOMIC_RELAXED, __HIP_MEMORY_SCOPE_AGENT); }
; #define XB_SPIN(cond, bar) do { unsigned _sp = 0; while (cond) { __builtin_amdgcn_s_sleep(1); \
;     if ((++_sp & 255u) == 0u) { if (xb_ld(&(bar)[XB_TMO])) break; if (_sp > XB_SPIN_CAP) { atomicAdd(&(bar)[XB_TMO], 1u); break; } } } } while (0)
; __device__ __forceinline__ void xcd_barrier(const XcdBarrier& b, int wave_id, int pair = -1) {
;     ...
;         } else {
;             XB_SPIN(xb_ld(&bar[XB_XGEN(b.x)]) == gen, bar);
;             __builtin_amdgcn_fence(__ATOMIC_ACQUIRE, "agent");
;             asm volatile("s_waitcnt vmcnt(0)" ::: "memory");
;         }
.LBB0_87:
	s_or_b64 exec, exec, s[10:11]
	s_waitcnt vmcnt(0)
	s_waitcnt vmcnt(0)

; __device__ __forceinline__ unsigned xb_ld(unsigned* p)              { return __hip_atomic_load(p, __ATOMIC_RELAXED, __HIP_MEMORY_SCOPE_AGENT); }
; __device__ __forceinline__ unsigned xb_add(unsigned* p, unsigned v) { return __hip_atomic_fetch_add(p, v, __ATOMIC_RELAXED, __HIP_MEMORY_SCOPE_AGENT); }
; #define XB_SPIN(cond, bar) do { unsigned _sp = 0; while (cond) { __builtin_amdgcn_s_sleep(1); \
;     if ((++_sp & 255u) == 0u) { if (xb_ld(&(bar)[XB_TMO])) break; if (_sp > XB_SPIN_CAP) { atomicAdd(&(bar)[XB_TMO], 1u); break; } } } } while (0)
; __device__ __forceinline__ void xcd_barrier(const XcdBarrier& b, int wave_id, int pair = -1) {
;     ...
;             if (og + 1u == (tg + 1u) * nx) xb_add(topg, 1u);
;             else XB_SPIN(xb_ld(topg) == tg, bar);
;             __builtin_amdgcn_fence(__ATOMIC_ACQUIRE, "agent");
;             xb_add(&bar[XB_XGEN(b.x)], 1u);
;             asm volatile("s_waitcnt vmcnt(0)" ::: "memory");
.LBB0_105:
	s_or_b64 exec, exec, s[8:9]
	s_mov_b64 s[8:9], exec
	v_mbcnt_lo_u32_b32 v0, s8, 0
	v_mbcnt_hi_u32_b32 v0, s9, v0
	v_cmp_eq_u32_e32 vcc, 0, v0
	s_and_saveexec_b64 s[10:11], vcc
	s_cbranch_execz .LBB0_107
	s_bcnt1_i32_b64 s3, s[8:9]
	v_mov_b32_e32 v0, 0x2000
	v_mov_b32_e32 v1, s3
	global_atomic_add v0, v1, s[6:7] offset:1024
.LBB0_107:
	s_or_b64 exec, exec, s[10:11]
	buffer_inv sc1
	s_waitcnt vmcnt(0)

; __device__ __forceinline__ unsigned xb_ld(unsigned* p)              { return __hip_atomic_load(p, __ATOMIC_RELAXED, __HIP_MEMORY_SCOPE_AGENT); }
; __device__ __forceinline__ unsigned xb_add(unsigned* p, unsigned v) { return __hip_atomic_fetch_add(p, v, __ATOMIC_RELAXED, __HIP_MEMORY_SCOPE_AGENT); }
; #define XB_SPIN(cond, bar) do { unsigned _sp = 0; while (cond) { __builtin_amdgcn_s_sleep(1); \
;     if ((++_sp & 255u) == 0u) { if (xb_ld(&(bar)[XB_TMO])) break; if (_sp > XB_SPIN_CAP) { atomicAdd(&(bar)[XB_TMO], 1u); break; } } } } while (0)
; __device__ __forceinline__ void xcd_barrier(const XcdBarrier& b, int wave_id, int pair = -1) {
;     ...
;         const unsigned old = xb_add(&bar[XB_XSUB(b.x)], 1u);
;         const unsigned gen = old / nloc;
;         if (old + 1u == (gen + 1u) * nloc) {
;             __builtin_amdgcn_fence(__ATOMIC_RELEASE, "agent");
;             asm volatile("s_waitcnt vmcnt(0)" ::: "memory");
;             unsigned* topw = pair < 0 ? &bar[XB_TOP] : &bar[XB_PTOP(pair)]; unsigned* topg = pair < 0 ? &bar[XB_TOPGEN] : &bar[XB_PTOPGEN(pair)];
;             if (pair >= 0) nx = 2u;
;             const unsigned og = xb_add(topw, 1u);
;             const unsigned tg = og / nx;
;             if (og + 1u == (tg + 1u) * nx) xb_add(topg, 1u);
;             else XB_SPIN(xb_ld(topg) == tg, bar);
;             __builtin_amdgcn_fence(__ATOMIC_ACQUIRE, "agent");
;             xb_add(&bar[XB_XGEN(b.x)], 1u);
;             asm volatile("s_waitcnt vmcnt(0)" ::: "memory");
;         } else {
;             XB_SPIN(xb_ld(&bar[XB_XGEN(b.x)]) == gen, bar);
;             __builtin_amdgcn_fence(__ATOMIC_ACQUIRE, "agent");
;             asm volatile("s_waitcnt vmcnt(0)" ::: "memory");
.LBB0_211:
	s_or_b64 exec, exec, s[10:11]
	v_cvt_f32_u32_e32 v5, v3
	s_waitcnt vmcnt(0)
	v_readfirstlane_b32 s4, v4
	v_sub_u32_e32 v4, 0, v3
	v_rcp_iflag_f32_e32 v5, v5
	v_add_u32_e32 v6, s4, v2
	v_mul_f32_e32 v5, 0x4f7ffffe, v5
	v_cvt_u32_f32_e32 v5, v5
	v_mul_lo_u32 v2, v4, v5
	v_mul_hi_u32 v2, v5, v2
	v_add_u32_e32 v2, v5, v2
	v_mul_hi_u32 v2, v6, v2
	v_mul_lo_u32 v4, v2, v3
	v_sub_u32_e32 v4, v6, v4
	v_add_u32_e32 v5, 1, v2
	v_cmp_ge_u32_e32 vcc, v4, v3
	s_nop 1
	v_cndmask_b32_e32 v2, v2, v5, vcc
	v_sub_u32_e32 v5, v4, v3
	v_cndmask_b32_e32 v4, v4, v5, vcc
	v_add_u32_e32 v5, 1, v2
	v_cmp_ge_u32_e32 vcc, v4, v3
	v_add_u32_e32 v4, 1, v6
	s_nop 0
	v_cndmask_b32_e32 v2, v2, v5, vcc
	v_mul_lo_u32 v5, v3, v2
	v_add_u32_e32 v3, v5, v3
	v_cmp_ne_u32_e32 vcc, v4, v3
	s_and_saveexec_b64 s[4:5], vcc
	s_xor_b64 s[4:5], exec, s[4:5]
	s_cbranch_execz .LBB0_225
	buffer_inv sc1
	v_mov_b32_e32 v0, 0x2000
	global_load_dword v0, v0, s[8:9] offset:1024 sc1
	s_add_u32 s14, s8, 0x2400
	s_addc_u32 s15, s9, 0
	s_waitcnt vmcnt(0)
	v_cmp_eq_u32_e32 vcc, v0, v2
	s_and_saveexec_b64 s[10:11], vcc
	s_cbranch_execz .LBB0_224
	s_add_u32 s12, s30, 0x4200
	s_addc_u32 s13, s31, 0
	s_mov_b32 s26, 1
	s_mov_b64 s[16:17], 0
	v_mov_b32_e32 v0, 0
	s_branch .LBB0_215

; __device__ __forceinline__ unsigned xb_ld(unsigned* p)              { return __hip_atomic_load(p, __ATOMIC_RELAXED, __HIP_MEMORY_SCOPE_AGENT); }
; #define XB_SPIN(cond, bar) do { unsigned _sp = 0; while (cond) { __builtin_amdgcn_s_sleep(1); \
;     if ((++_sp & 255u) == 0u) { if (xb_ld(&(bar)[XB_TMO])) break; if (_sp > XB_SPIN_CAP) { atomicAdd(&(bar)[XB_TMO], 1u); break; } } } } while (0)
; __device__ __forceinline__ void xcd_barrier(const XcdBarrier& b, int wave_id, int pair = -1) {
;     ...
;         } else {
;             XB_SPIN(xb_ld(&bar[XB_XGEN(b.x)]) == gen, bar);
;             __builtin_amdgcn_fence(__ATOMIC_ACQUIRE, "agent");
;             asm volatile("s_waitcnt vmcnt(0)" ::: "memory");
;         }
.LBB0_224:
	s_or_b64 exec, exec, s[10:11]
	s_waitcnt vmcnt(0) lgkmcnt(0)
	s_waitcnt vmcnt(0)

; __device__ __forceinline__ unsigned xb_ld(unsigned* p)              { return __hip_atomic_load(p, __ATOMIC_RELAXED, __HIP_MEMORY_SCOPE_AGENT); }
; __device__ __forceinline__ unsigned xb_add(unsigned* p, unsigned v) { return __hip_atomic_fetch_add(p, v, __ATOMIC_RELAXED, __HIP_MEMORY_SCOPE_AGENT); }
; #define XB_SPIN(cond, bar) do { unsigned _sp = 0; while (cond) { __builtin_amdgcn_s_sleep(1); \
;     if ((++_sp & 255u) == 0u) { if (xb_ld(&(bar)[XB_TMO])) break; if (_sp > XB_SPIN_CAP) { atomicAdd(&(bar)[XB_TMO], 1u); break; } } } } while (0)
; __device__ __forceinline__ void xcd_barrier(const XcdBarrier& b, int wave_id, int pair = -1) {
;     ...
;             if (og + 1u == (tg + 1u) * nx) xb_add(topg, 1u);
;             else XB_SPIN(xb_ld(topg) == tg, bar);
;             __builtin_amdgcn_fence(__ATOMIC_ACQUIRE, "agent");
;             xb_add(&bar[XB_XGEN(b.x)], 1u);
;             asm volatile("s_waitcnt vmcnt(0)" ::: "memory");
.LBB0_242:
	s_or_b64 exec, exec, s[4:5]
	s_mov_b64 s[4:5], exec
	v_mbcnt_lo_u32_b32 v0, s4, 0
	v_mbcnt_hi_u32_b32 v0, s5, v0
	v_cmp_eq_u32_e32 vcc, 0, v0
	s_and_saveexec_b64 s[10:11], vcc
	s_cbranch_execz .LBB0_244
	s_bcnt1_i32_b64 s3, s[4:5]
	v_mov_b32_e32 v0, 0x2000
	v_mov_b32_e32 v1, s3
	global_atomic_add v0, v1, s[8:9] offset:1024

; __device__ __forceinline__ unsigned xb_ld(unsigned* p)              { return __hip_atomic_load(p, __ATOMIC_RELAXED, __HIP_MEMORY_SCOPE_AGENT); }
; __device__ __forceinline__ unsigned xb_add(unsigned* p, unsigned v) { return __hip_atomic_fetch_add(p, v, __ATOMIC_RELAXED, __HIP_MEMORY_SCOPE_AGENT); }
; #define XB_SPIN(cond, bar) do { unsigned _sp = 0; while (cond) { __builtin_amdgcn_s_sleep(1); \
;     if ((++_sp & 255u) == 0u) { if (xb_ld(&(bar)[XB_TMO])) break; if (_sp > XB_SPIN_CAP) { atomicAdd(&(bar)[XB_TMO], 1u); break; } } } } while (0)
; __device__ __forceinline__ void xcd_barrier(const XcdBarrier& b, int wave_id, int pair = -1) {
;     ...
;         const unsigned old = xb_add(&bar[XB_XSUB(b.x)], 1u);
;         const unsigned gen = old / nloc;
;         if (old + 1u == (gen + 1u) * nloc) {
;             __builtin_amdgcn_fence(__ATOMIC_RELEASE, "agent");
;             asm volatile("s_waitcnt vmcnt(0)" ::: "memory");
;             unsigned* topw = pair < 0 ? &bar[XB_TOP] : &bar[XB_PTOP(pair)]; unsigned* topg = pair < 0 ? &bar[XB_TOPGEN] : &bar[XB_PTOPGEN(pair)];
;             if (pair >= 0) nx = 2u;
;             const unsigned og = xb_add(topw, 1u);
;             const unsigned tg = og / nx;
;             if (og + 1u == (tg + 1u) * nx) xb_add(topg, 1u);
;             else XB_SPIN(xb_ld(topg) == tg, bar);
;             __builtin_amdgcn_fence(__ATOMIC_ACQUIRE, "agent");
;             xb_add(&bar[XB_XGEN(b.x)], 1u);
;             asm volatile("s_waitcnt vmcnt(0)" ::: "memory");
;         } else {
;             XB_SPIN(xb_ld(&bar[XB_XGEN(b.x)]) == gen, bar);
;             __builtin_amdgcn_fence(__ATOMIC_ACQUIRE, "agent");
;             asm volatile("s_waitcnt vmcnt(0)" ::: "memory");
.LBB0_515:
	s_or_b64 exec, exec, s[10:11]
	v_cvt_f32_u32_e32 v4, v2
	s_waitcnt vmcnt(0)
	v_readfirstlane_b32 s8, v3
	v_sub_u32_e32 v3, 0, v2
	v_rcp_iflag_f32_e32 v4, v4
	v_add_u32_e32 v5, s8, v1
	v_mul_f32_e32 v4, 0x4f7ffffe, v4
	v_cvt_u32_f32_e32 v4, v4
	v_mul_lo_u32 v1, v3, v4
	v_mul_hi_u32 v1, v4, v1
	v_add_u32_e32 v1, v4, v1
	v_mul_hi_u32 v1, v5, v1
	v_mul_lo_u32 v3, v1, v2
	v_sub_u32_e32 v3, v5, v3
	v_add_u32_e32 v4, 1, v1
	v_cmp_ge_u32_e32 vcc, v3, v2
	s_nop 1
	v_cndmask_b32_e32 v1, v1, v4, vcc
	v_sub_u32_e32 v4, v3, v2
	v_cndmask_b32_e32 v3, v3, v4, vcc
	v_add_u32_e32 v4, 1, v1
	v_cmp_ge_u32_e32 vcc, v3, v2
	v_add_u32_e32 v3, 1, v5
	s_nop 0
	v_cndmask_b32_e32 v1, v1, v4, vcc
	v_mul_lo_u32 v4, v2, v1
	v_add_u32_e32 v2, v4, v2
	v_cmp_ne_u32_e32 vcc, v3, v2
	s_and_saveexec_b64 s[8:9], vcc
	s_xor_b64 s[8:9], exec, s[8:9]
	s_cbranch_execz .LBB0_529
	s_waitcnt lgkmcnt(0)
	buffer_inv sc1
	v_mov_b32_e32 v0, 0x2000
	global_load_dword v0, v0, s[6:7] offset:1024 sc1
	s_add_u32 s14, s6, 0x2400
	s_addc_u32 s15, s7, 0
	s_waitcnt vmcnt(0)
	v_cmp_eq_u32_e32 vcc, v0, v1
	s_and_saveexec_b64 s[10:11], vcc
	s_cbranch_execz .LBB0_528
	s_add_u32 s12, s30, 0x4200
	s_addc_u32 s13, s31, 0
	s_mov_b32 s26, 1
	s_mov_b64 s[16:17], 0
	v_mov_b32_e32 v0, 0
	s_branch .LBB0_519

; __device__ __forceinline__ unsigned xb_ld(unsigned* p)              { return __hip_atomic_load(p, __ATOMIC_RELAXED, __HIP_MEMORY_SCOPE_AGENT); }
; __device__ __forceinline__ unsigned xb_add(unsigned* p, unsigned v) { return __hip_atomic_fetch_add(p, v, __ATOMIC_RELAXED, __HIP_MEMORY_SCOPE_AGENT); }
; #define XB_SPIN(cond, bar) do { unsigned _sp = 0; while (cond) { __builtin_amdgcn_s_sleep(1); \
;     if ((++_sp & 255u) == 0u) { if (xb_ld(&(bar)[XB_TMO])) break; if (_sp > XB_SPIN_CAP) { atomicAdd(&(bar)[XB_TMO], 1u); break; } } } } while (0)
; __device__ __forceinline__ void xcd_barrier(const XcdBarrier& b, int wave_id, int pair = -1) {
;     ...
;             if (og + 1u == (tg + 1u) * nx) xb_add(topg, 1u);
;             else XB_SPIN(xb_ld(topg) == tg, bar);
;             __builtin_amdgcn_fence(__ATOMIC_ACQUIRE, "agent");
;             xb_add(&bar[XB_XGEN(b.x)], 1u);
;             asm volatile("s_waitcnt vmcnt(0)" ::: "memory");
.LBB0_546:
	s_or_b64 exec, exec, s[8:9]
	s_mov_b64 s[8:9], exec
	v_mbcnt_lo_u32_b32 v0, s8, 0
	v_mbcnt_hi_u32_b32 v0, s9, v0
	v_cmp_eq_u32_e32 vcc, 0, v0
	s_and_saveexec_b64 s[10:11], vcc
	s_cbranch_execz .LBB0_548
	s_bcnt1_i32_b64 s8, s[8:9]
	v_mov_b32_e32 v0, 0x2000
	v_mov_b32_e32 v1, s8
	global_atomic_add v0, v1, s[6:7] offset:1024

; __device__ __forceinline__ unsigned xb_ld(unsigned* p)              { return __hip_atomic_load(p, __ATOMIC_RELAXED, __HIP_MEMORY_SCOPE_AGENT); }
; __device__ __forceinline__ unsigned xb_add(unsigned* p, unsigned v) { return __hip_atomic_fetch_add(p, v, __ATOMIC_RELAXED, __HIP_MEMORY_SCOPE_AGENT); }
; #define XB_SPIN(cond, bar) do { unsigned _sp = 0; while (cond) { __builtin_amdgcn_s_sleep(1); \
;     if ((++_sp & 255u) == 0u) { if (xb_ld(&(bar)[XB_TMO])) break; if (_sp > XB_SPIN_CAP) { atomicAdd(&(bar)[XB_TMO], 1u); break; } } } } while (0)
; __device__ __forceinline__ void xcd_local_barrier(unsigned* w, unsigned n, unsigned* tmo, int wave_id) {
;     ...
;         (void)xb_add(w, 1u);
;         XB_SPIN(xb_ld(w) < n, tmo - XB_TMO);
;         __builtin_amdgcn_fence(__ATOMIC_ACQUIRE, "agent");
;         asm volatile("s_waitcnt vmcnt(0)" ::: "memory");
.LBB0_555:
	s_or_b64 exec, exec, s[10:11]
	buffer_inv sc1
	v_mov_b32_e32 v0, 0
	global_load_dword v1, v0, s[6:7] sc1
	s_ashr_i32 s3, s3, 3
	s_waitcnt vmcnt(0)
	v_cmp_le_u32_e32 vcc, s3, v1
	s_cbranch_vccnz .LBB0_568
	s_add_u32 s8, s30, 0x4200
	s_addc_u32 s9, s31, 0
	s_mov_b32 s16, 1
	s_branch .LBB0_558

; __device__ __forceinline__ unsigned xb_ld(unsigned* p)              { return __hip_atomic_load(p, __ATOMIC_RELAXED, __HIP_MEMORY_SCOPE_AGENT); }
; #define XB_SPIN(cond, bar) do { unsigned _sp = 0; while (cond) { __builtin_amdgcn_s_sleep(1); \
;     if ((++_sp & 255u) == 0u) { if (xb_ld(&(bar)[XB_TMO])) break; if (_sp > XB_SPIN_CAP) { atomicAdd(&(bar)[XB_TMO], 1u); break; } } } } while (0)
; __device__ __forceinline__ void xcd_local_barrier(unsigned* w, unsigned n, unsigned* tmo, int wave_id) {
;     ...
;         XB_SPIN(xb_ld(w) < n, tmo - XB_TMO);
;         __builtin_amdgcn_fence(__ATOMIC_ACQUIRE, "agent");
;         asm volatile("s_waitcnt vmcnt(0)" ::: "memory");
;     }
.LBB0_568:
	s_waitcnt vmcnt(0)
	s_waitcnt vmcnt(0)

; __device__ __forceinline__ unsigned xb_ld(unsigned* p)              { return __hip_atomic_load(p, __ATOMIC_RELAXED, __HIP_MEMORY_SCOPE_AGENT); }
; __device__ __forceinline__ unsigned xb_add(unsigned* p, unsigned v) { return __hip_atomic_fetch_add(p, v, __ATOMIC_RELAXED, __HIP_MEMORY_SCOPE_AGENT); }
; #define XB_SPIN(cond, bar) do { unsigned _sp = 0; while (cond) { __builtin_amdgcn_s_sleep(1); \
;     if ((++_sp & 255u) == 0u) { if (xb_ld(&(bar)[XB_TMO])) break; if (_sp > XB_SPIN_CAP) { atomicAdd(&(bar)[XB_TMO], 1u); break; } } } } while (0)
; __device__ __forceinline__ void xcd_barrier(const XcdBarrier& b, int wave_id, int pair = -1) {
;     ...
;         const unsigned old = xb_add(&bar[XB_XSUB(b.x)], 1u);
;         const unsigned gen = old / nloc;
;         if (old + 1u == (gen + 1u) * nloc) {
;             __builtin_amdgcn_fence(__ATOMIC_RELEASE, "agent");
;             asm volatile("s_waitcnt vmcnt(0)" ::: "memory");
;             unsigned* topw = pair < 0 ? &bar[XB_TOP] : &bar[XB_PTOP(pair)]; unsigned* topg = pair < 0 ? &bar[XB_TOPGEN] : &bar[XB_PTOPGEN(pair)];
;             if (pair >= 0) nx = 2u;
;             const unsigned og = xb_add(topw, 1u);
;             const unsigned tg = og / nx;
;             if (og + 1u == (tg + 1u) * nx) xb_add(topg, 1u);
;             else XB_SPIN(xb_ld(topg) == tg, bar);
;             __builtin_amdgcn_fence(__ATOMIC_ACQUIRE, "agent");
;             xb_add(&bar[XB_XGEN(b.x)], 1u);
;             asm volatile("s_waitcnt vmcnt(0)" ::: "memory");
;         } else {
;             XB_SPIN(xb_ld(&bar[XB_XGEN(b.x)]) == gen, bar);
;             __builtin_amdgcn_fence(__ATOMIC_ACQUIRE, "agent");
;             asm volatile("s_waitcnt vmcnt(0)" ::: "memory");
.LBB0_2045:
	s_or_b64 exec, exec, s[6:7]
	v_cvt_f32_u32_e32 v4, v2
	s_waitcnt vmcnt(0)
	v_readfirstlane_b32 s4, v3
	v_sub_u32_e32 v3, 0, v2
	v_rcp_iflag_f32_e32 v4, v4
	v_add_u32_e32 v5, s4, v1
	v_mul_f32_e32 v4, 0x4f7ffffe, v4
	v_cvt_u32_f32_e32 v4, v4
	v_mul_lo_u32 v1, v3, v4
	v_mul_hi_u32 v1, v4, v1
	v_add_u32_e32 v1, v4, v1
	v_mul_hi_u32 v1, v5, v1
	v_mul_lo_u32 v3, v1, v2
	v_sub_u32_e32 v3, v5, v3
	v_add_u32_e32 v4, 1, v1
	v_cmp_ge_u32_e32 vcc, v3, v2
	s_nop 1
	v_cndmask_b32_e32 v1, v1, v4, vcc
	v_sub_u32_e32 v4, v3, v2
	v_cndmask_b32_e32 v3, v3, v4, vcc
	v_add_u32_e32 v4, 1, v1
	v_cmp_ge_u32_e32 vcc, v3, v2
	v_add_u32_e32 v3, 1, v5
	s_nop 0
	v_cndmask_b32_e32 v1, v1, v4, vcc
	v_mul_lo_u32 v4, v2, v1
	v_add_u32_e32 v2, v4, v2
	v_cmp_ne_u32_e32 vcc, v3, v2
	s_and_saveexec_b64 s[4:5], vcc
	s_xor_b64 s[4:5], exec, s[4:5]
	s_cbranch_execz .LBB0_2059
	s_waitcnt lgkmcnt(0)
	buffer_inv sc1
	v_mov_b32_e32 v0, 0x2000
	global_load_dword v0, v0, s[2:3] offset:1024 sc1
	s_add_u32 s10, s2, 0x2400
	s_addc_u32 s11, s3, 0
	s_waitcnt vmcnt(0)
	v_cmp_eq_u32_e32 vcc, v0, v1
	s_and_saveexec_b64 s[6:7], vcc
	s_cbranch_execz .LBB0_2058
	s_add_u32 s8, s30, 0x4200
	s_addc_u32 s9, s31, 0
	s_mov_b32 s22, 1
	s_mov_b64 s[12:13], 0
	v_mov_b32_e32 v0, 0
	s_branch .LBB0_2049

; __device__ __forceinline__ unsigned xb_ld(unsigned* p)              { return __hip_atomic_load(p, __ATOMIC_RELAXED, __HIP_MEMORY_SCOPE_AGENT); }
; #define XB_SPIN(cond, bar) do { unsigned _sp = 0; while (cond) { __builtin_amdgcn_s_sleep(1); \
;     if ((++_sp & 255u) == 0u) { if (xb_ld(&(bar)[XB_TMO])) break; if (_sp > XB_SPIN_CAP) { atomicAdd(&(bar)[XB_TMO], 1u); break; } } } } while (0)
; __device__ __forceinline__ void xcd_barrier(const XcdBarrier& b, int wave_id, int pair = -1) {
;     ...
;         } else {
;             XB_SPIN(xb_ld(&bar[XB_XGEN(b.x)]) == gen, bar);
;             __builtin_amdgcn_fence(__ATOMIC_ACQUIRE, "agent");
;             asm volatile("s_waitcnt vmcnt(0)" ::: "memory");
;         }
.LBB0_2058:
	s_or_b64 exec, exec, s[6:7]
	s_waitcnt vmcnt(0)
	s_waitcnt vmcnt(0)

; __device__ __forceinline__ unsigned xb_ld(unsigned* p)              { return __hip_atomic_load(p, __ATOMIC_RELAXED, __HIP_MEMORY_SCOPE_AGENT); }
; __device__ __forceinline__ unsigned xb_add(unsigned* p, unsigned v) { return __hip_atomic_fetch_add(p, v, __ATOMIC_RELAXED, __HIP_MEMORY_SCOPE_AGENT); }
; #define XB_SPIN(cond, bar) do { unsigned _sp = 0; while (cond) { __builtin_amdgcn_s_sleep(1); \
;     if ((++_sp & 255u) == 0u) { if (xb_ld(&(bar)[XB_TMO])) break; if (_sp > XB_SPIN_CAP) { atomicAdd(&(bar)[XB_TMO], 1u); break; } } } } while (0)
; __device__ __forceinline__ void xcd_barrier(const XcdBarrier& b, int wave_id, int pair = -1) {
;     ...
;             if (og + 1u == (tg + 1u) * nx) xb_add(topg, 1u);
;             else XB_SPIN(xb_ld(topg) == tg, bar);
;             __builtin_amdgcn_fence(__ATOMIC_ACQUIRE, "agent");
;             xb_add(&bar[XB_XGEN(b.x)], 1u);
;             asm volatile("s_waitcnt vmcnt(0)" ::: "memory");
.LBB0_2076:
	s_or_b64 exec, exec, s[4:5]
	s_mov_b64 s[4:5], exec
	v_mbcnt_lo_u32_b32 v0, s4, 0
	v_mbcnt_hi_u32_b32 v0, s5, v0
	v_cmp_eq_u32_e32 vcc, 0, v0
	s_and_saveexec_b64 s[6:7], vcc
	s_cbranch_execz .LBB0_2078
	s_bcnt1_i32_b64 s4, s[4:5]
	v_mov_b32_e32 v0, 0x2000
	v_mov_b32_e32 v1, s4
	global_atomic_add v0, v1, s[2:3] offset:1024
.LBB0_2078:
	s_or_b64 exec, exec, s[6:7]
	buffer_inv sc1
	s_waitcnt vmcnt(0)
